# FT also pulls its tile's k_final slot count into L2
# baseline (speedup 1.0000x reference)
_Z6k_iterILb0ELb1EEvPKfS1_PKiPK15HIP_vector_typeIfLj4EES7_S1_S1_S3_S1_PfS8_S1_S3_PDF16_PS5_SA_PiSA_SB_:
	s_and_b32 s38, s0, 0xfffff000
	s_mov_b32 s39, s1
	s_load_dwordx2 s[8:9], s[0:1], 0x80
	s_load_dwordx4 s[4:7], s[0:1], 0x70
	s_load_dwordx4 s[16:19], s[0:1], 0x40
	s_load_dwordx2 s[22:23], s[0:1], 0x50
	s_load_dwordx2 s[42:43], s[0:1], 0x88
	s_load_dwordx2 s[44:45], s[0:1], 0x90
	v_readfirstlane_b32 s12, v0
	v_cmp_gt_u32_e64 s[14:15], 64, v0
	v_lshlrev_b32_e32 v1, 2, v0
	s_and_saveexec_b64 s[10:11], s[14:15]
	v_mov_b32_e32 v2, 0
	ds_write_b32 v1, v2 offset:5152
	s_or_b64 exec, exec, s[10:11]
	s_lshl_b32 s3, s2, 5
	s_and_b32 s3, s3, 0xe0
	s_lshr_b32 s2, s2, 3
	s_add_i32 s2, s3, s2
	s_lshl_b32 s29, s2, 6
	v_and_b32_e32 v2, 31, v0
	v_or_b32_e32 v4, s29, v2
	v_mov_b32_e32 v5, 0
	s_lshr_b32 s30, s12, 6
	s_lshl_b32 s32, s30, 2
	s_lshr_b32 s32, 0x73261540, s32
	s_lshl_b32 s32, s32, 5
	s_and_b32 s32, s32, 0xe0
	v_or_b32_e32 v176, s32, v2
	v_lshlrev_b32_e32 v177, 4, v176
	v_add_u32_e32 v178, 0x1000, v177
	v_add_u32_e32 v179, 0x2000, v177
	v_add_u32_e32 v180, 0x3000, v177
	v_add_u32_e32 v181, 0x4000, v177
	v_add_u32_e32 v182, 0x5000, v177
	s_mov_b32 s3, 0
	s_lshl_b64 s[34:35], s[2:3], 16
	s_lshl_b32 s33, s2, 2
	s_waitcnt lgkmcnt(0)
	s_load_dword s26, s[8:9], s33 offset:0x0
	s_add_u32 s20, s4, s34
	s_addc_u32 s21, s5, s35
	v_lshl_add_u64 v[4:5], v[4:5], 4, s[6:7]
	global_load_dwordx3 v[30:32], v[4:5], off
	global_load_dwordx3 v[26:28], v[4:5], off offset:512
	global_load_dwordx4 v[2:5], v177, s[20:21]
	global_load_dwordx4 v[6:9], v178, s[20:21]
	global_load_dwordx4 v[10:13], v179, s[20:21]
	global_load_dwordx4 v[14:17], v180, s[20:21]
	global_load_dwordx4 v[18:21], v181, s[20:21]
	global_load_dwordx4 v[22:25], v182, s[20:21]
	v_and_b32_e32 v38, 63, v0
	v_mov_b32_e32 v29, 0xff800000
	v_cmp_gt_u32_e64 s[0:1], 32, v38
	s_waitcnt lgkmcnt(0)
	s_cmpk_gt_i32 s26, 0x600
	s_cselect_b64 s[24:25], -1, 0
	s_cmpk_lt_i32 s26, 0x601
	s_cbranch_scc1 .LBB4_6
	s_and_saveexec_b64 s[8:9], s[14:15]
	s_cbranch_execz .LBB4_5
	v_or_b32_e32 v178, s29, v0
	v_mov_b32_e32 v179, 0
	v_lshl_add_u64 v[178:179], v[178:179], 4, s[6:7]
	global_load_dwordx4 v[178:181], v[178:179], off
	v_lshlrev_b32_e32 v177, 4, v0
	s_waitcnt vmcnt(0)
	ds_write_b128 v177, v[178:181] offset:2080

.LBB4_39:
	s_waitcnt vmcnt(5)
	v_rcp_f32_e32 v2, v133
	s_waitcnt vmcnt(4)
	v_rcp_f32_e32 v3, v132
	s_waitcnt vmcnt(3)
	v_rcp_f32_e32 v4, v131
	v_cmp_lt_f32_e32 vcc, 0, v133
	s_waitcnt vmcnt(2)
	v_rcp_f32_e32 v5, v130
	s_waitcnt vmcnt(1)
	v_rcp_f32_e32 v6, v129
	v_cndmask_b32_e32 v2, 0, v2, vcc
	v_cmp_lt_f32_e32 vcc, 0, v132
	s_waitcnt vmcnt(0)
	v_rcp_f32_e32 v7, v128
	s_getpc_b64 s[36:37]
	s_sub_u32 s36, s36, 0x9248
	s_subb_u32 s37, s37, 0
	v_lshlrev_b32_e32 v183, 6, v0
	v_min_u32_e32 v183, 0x1980, v183
	global_load_dword v183, v183, s[36:37]
	v_lshlrev_b32_e32 v182, 6, v38
	global_load_dword v182, v182, s[38:39]
	s_lshr_b32 s46, s29, 4
	s_load_dword s46, s[44:45], s46 offset:0x0
	s_lshl_b32 s40, s29, 10
	s_add_u32 s40, s42, s40
	s_addc_u32 s41, s43, 0
	v_lshlrev_b32_e32 v181, 6, v0
	v_and_b32_e32 v181, 0x7fc0, v181
	global_load_dword v181, v181, s[40:41]
	s_mov_b32 s4, 0x42c80000
	v_cndmask_b32_e32 v3, 0, v3, vcc
	v_cmp_lt_f32_e32 vcc, 0, v131
	v_cmp_ngt_f32_e64 s[2:3], s4, v3
	s_mov_b64 s[6:7], 0
	v_cndmask_b32_e32 v4, 0, v4, vcc
	v_cmp_lt_f32_e32 vcc, 0, v130
	s_nop 1
	v_cndmask_b32_e32 v5, 0, v5, vcc
	v_cmp_lt_f32_e32 vcc, 0, v129
	s_nop 1
	v_cndmask_b32_e32 v6, 0, v6, vcc
	v_cmp_lt_f32_e32 vcc, 0, v128
	s_nop 1
	v_cndmask_b32_e32 v7, 0, v7, vcc
	v_cmp_ngt_f32_e32 vcc, s4, v2
	s_or_b64 s[2:3], vcc, s[2:3]
	v_cmp_ngt_f32_e32 vcc, s4, v4
	s_or_b64 s[2:3], s[2:3], vcc
	v_cmp_ngt_f32_e32 vcc, s4, v5
	s_or_b64 s[2:3], s[2:3], vcc
	v_cmp_ngt_f32_e32 vcc, s4, v6
	s_or_b64 s[2:3], s[2:3], vcc
	v_cmp_ngt_f32_e32 vcc, s4, v7
	s_or_b64 s[2:3], s[2:3], vcc
	v_cndmask_b32_e64 v8, 0, 1, s[2:3]
	v_cmp_ne_u32_e32 vcc, 0, v8
	s_cmp_eq_u64 vcc, 0
	s_cselect_b64 s[2:3], -1, 0
	v_cndmask_b32_e64 v8, 0, 1, s[2:3]
	s_nop 0
	v_readfirstlane_b32 s2, v8
	s_bitcmp0_b32 s2, 0
	s_cbranch_scc0 .LBB4_45
	s_cmp_lt_i32 s28, 4
	s_cbranch_scc1 .LBB4_46
	s_cmp_gt_i32 s28, 4
	s_cbranch_scc0 .LBB4_47
	s_mov_b64 s[4:5], -1
	v_mov_b32_e32 v8, 0
	s_cmp_gt_i32 s28, 5
	v_mov_b32_e32 v167, 0
	v_mov_b32_e32 v166, 0
	v_mov_b32_e32 v165, 0
	v_mov_b32_e32 v164, 0
	v_mov_b32_e32 v162, 0
	v_mov_b32_e32 v160, 0
	v_mov_b32_e32 v159, 0
	v_mov_b32_e32 v157, 0
	v_mov_b32_e32 v151, 0
	v_mov_b32_e32 v149, 0
	v_mov_b32_e32 v147, 0
	v_mov_b32_e32 v146, 0
	v_mov_b32_e32 v144, 0
	v_mov_b32_e32 v143, 0
	v_mov_b32_e32 v152, 0
	v_mov_b32_e32 v153, 0
	v_mov_b32_e32 v154, 0
	v_mov_b32_e32 v155, 0
	v_mov_b32_e32 v156, 0
	v_mov_b32_e32 v158, 0
	v_mov_b32_e32 v161, 0
	v_mov_b32_e32 v163, 0
	v_mov_b32_e32 v168, 0
	v_mov_b32_e32 v169, 0
	v_mov_b32_e32 v170, 0
	v_mov_b32_e32 v171, 0
	v_mov_b32_e32 v172, 0
	v_mov_b32_e32 v173, 0
	v_mov_b32_e32 v174, 0
	v_mov_b32_e32 v145, 0
	v_mov_b32_e32 v148, 0
	v_mov_b32_e32 v150, 0
	s_cbranch_scc0 .LBB4_50
	s_cmp_eq_u32 s28, 6
	s_cbranch_scc0 .LBB4_49
	v_mov_b32_e32 v145, 0
	v_mov_b32_e32 v148, 0
	v_mov_b32_e32 v150, 0
	v_mov_b32_e32 v143, 0
	v_mov_b32_e32 v144, 0
	v_mov_b32_e32 v146, 0
	v_mov_b32_e32 v147, 0
	v_mov_b32_e32 v149, 0
	v_mov_b32_e32 v151, 0
	v_mov_b32_e32 v152, 0
	v_mov_b32_e32 v153, 0
	v_mov_b32_e32 v154, 0
	v_mov_b32_e32 v155, 0
	v_mov_b32_e32 v156, 0
	v_mov_b32_e32 v158, 0
	v_mov_b32_e32 v161, 0
	v_mov_b32_e32 v163, 0
	v_mov_b32_e32 v157, 0
	v_mov_b32_e32 v159, 0
	v_mov_b32_e32 v160, 0
	v_mov_b32_e32 v162, 0
	v_mov_b32_e32 v164, 0
	v_mov_b32_e32 v165, 0
	v_mov_b32_e32 v166, 0
	v_mov_b32_e32 v167, 0
	v_mov_b32_e32 v168, 0
	v_mov_b32_e32 v169, 0
	v_mov_b32_e32 v170, 0
	v_mov_b32_e32 v171, 0
	v_mov_b32_e32 v172, 0
	v_mov_b32_e32 v173, 0
	v_mov_b32_e32 v174, 0
	v_fma_mix_f32 v148, v43, v7, v148 op_sel_hi:[1,0,0]
	v_fma_mix_f32 v150, v45, v7, v150 op_sel_hi:[1,0,0]
	v_fma_mix_f32 v143, v50, v7, v143 op_sel_hi:[1,0,0]
	v_fma_mix_f32 v144, v54, v7, v144 op_sel_hi:[1,0,0]
	v_fma_mix_f32 v146, v58, v7, v146 op_sel_hi:[1,0,0]
	v_fma_mix_f32 v147, v61, v7, v147 op_sel_hi:[1,0,0]
	v_fma_mix_f32 v149, v64, v7, v149 op_sel_hi:[1,0,0]
	v_fma_mix_f32 v151, v66, v7, v151 op_sel_hi:[1,0,0]
	v_fma_mix_f32 v152, v43, v7, v152 op_sel:[1,0,0] op_sel_hi:[1,0,0]
	v_fma_mix_f32 v153, v45, v7, v153 op_sel:[1,0,0] op_sel_hi:[1,0,0]
	v_fma_mix_f32 v154, v50, v7, v154 op_sel:[1,0,0] op_sel_hi:[1,0,0]
	v_fma_mix_f32 v155, v54, v7, v155 op_sel:[1,0,0] op_sel_hi:[1,0,0]
	v_fma_mix_f32 v156, v58, v7, v156 op_sel:[1,0,0] op_sel_hi:[1,0,0]
	v_fma_mix_f32 v158, v61, v7, v158 op_sel:[1,0,0] op_sel_hi:[1,0,0]
	v_fma_mix_f32 v161, v64, v7, v161 op_sel:[1,0,0] op_sel_hi:[1,0,0]
	v_fma_mix_f32 v163, v66, v7, v163 op_sel:[1,0,0] op_sel_hi:[1,0,0]
	v_fma_mix_f32 v157, v72, v7, v157 op_sel_hi:[1,0,0]
	v_fma_mix_f32 v159, v76, v7, v159 op_sel_hi:[1,0,0]
	v_fma_mix_f32 v160, v83, v7, v160 op_sel_hi:[1,0,0]
	v_fma_mix_f32 v162, v85, v7, v162 op_sel_hi:[1,0,0]
	v_fma_mix_f32 v164, v89, v7, v164 op_sel_hi:[1,0,0]
	v_fma_mix_f32 v165, v92, v7, v165 op_sel_hi:[1,0,0]
	v_fma_mix_f32 v166, v95, v7, v166 op_sel_hi:[1,0,0]
	v_fma_mix_f32 v167, v96, v7, v167 op_sel_hi:[1,0,0]
	v_fma_mix_f32 v168, v72, v7, v168 op_sel:[1,0,0] op_sel_hi:[1,0,0]
	v_fma_mix_f32 v169, v76, v7, v169 op_sel:[1,0,0] op_sel_hi:[1,0,0]
	v_fma_mix_f32 v170, v83, v7, v170 op_sel:[1,0,0] op_sel_hi:[1,0,0]
	v_fma_mix_f32 v171, v85, v7, v171 op_sel:[1,0,0] op_sel_hi:[1,0,0]
	v_fma_mix_f32 v172, v89, v7, v172 op_sel:[1,0,0] op_sel_hi:[1,0,0]
	v_fma_mix_f32 v173, v92, v7, v173 op_sel:[1,0,0] op_sel_hi:[1,0,0]
	v_fma_mix_f32 v174, v95, v7, v174 op_sel:[1,0,0] op_sel_hi:[1,0,0]
	v_fma_mix_f32 v145, v96, v7, v145 op_sel:[1,0,0] op_sel_hi:[1,0,0]
	s_branch .LBB4_50

amdhsa.kernels:
  - .agpr_count:     0
    .args:
      - .actual_access:  read_only
        .address_space:  global
        .offset:         0
        .size:           8
        .value_kind:     global_buffer
      - .actual_access:  read_only
        .address_space:  global
        .offset:         8
        .size:           8
        .value_kind:     global_buffer
      - .actual_access:  read_only
        .address_space:  global
        .offset:         16
        .size:           8
        .value_kind:     global_buffer
      - .actual_access:  read_only
        .address_space:  global
        .offset:         24
        .size:           8
        .value_kind:     global_buffer
      - .actual_access:  write_only
        .address_space:  global
        .offset:         32
        .size:           8
        .value_kind:     global_buffer
      - .actual_access:  write_only
        .address_space:  global
        .offset:         40
        .size:           8
        .value_kind:     global_buffer
      - .actual_access:  write_only
        .address_space:  global
        .offset:         48
        .size:           8
        .value_kind:     global_buffer
      - .actual_access:  write_only
        .address_space:  global
        .offset:         56
        .size:           8
        .value_kind:     global_buffer
      - .actual_access:  write_only
        .address_space:  global
        .offset:         64
        .size:           8
        .value_kind:     global_buffer
      - .actual_access:  write_only
        .address_space:  global
        .offset:         72
        .size:           8
        .value_kind:     global_buffer
      - .actual_access:  write_only
        .address_space:  global
        .offset:         80
        .size:           8
        .value_kind:     global_buffer
      - .actual_access:  write_only
        .address_space:  global
        .offset:         88
        .size:           8
        .value_kind:     global_buffer
      - .actual_access:  write_only
        .address_space:  global
        .offset:         96
        .size:           8
        .value_kind:     global_buffer
      - .actual_access:  write_only
        .address_space:  global
        .offset:         104
        .size:           8
        .value_kind:     global_buffer
      - .actual_access:  write_only
        .address_space:  global
        .offset:         112
        .size:           8
        .value_kind:     global_buffer
    .group_segment_fixed_size: 67584
    .kernarg_segment_align: 8
    .kernarg_segment_size: 120
    .language:       OpenCL C
    .language_version:
      - 2
      - 0
    .max_flat_workgroup_size: 1024
    .name:           _Z6k_sortPKfS0_PKiS2_PiP15HIP_vector_typeIfLj4EEPfS7_S3_S7_S7_S3_S3_S6_S6_
    .private_segment_fixed_size: 0
    .sgpr_count:     58
    .sgpr_spill_count: 0
    .symbol:         _Z6k_sortPKfS0_PKiS2_PiP15HIP_vector_typeIfLj4EEPfS7_S3_S7_S7_S3_S3_S6_S6_.kd
    .uniform_work_group_size: 1
    .uses_dynamic_stack: false
    .vgpr_count:     48
    .vgpr_spill_count: 0
    .wavefront_size: 64
  - .agpr_count:     0
    .args:
      - .actual_access:  read_only
        .address_space:  global
        .offset:         0
        .size:           8
        .value_kind:     global_buffer
      - .actual_access:  read_only
        .address_space:  global
        .offset:         8
        .size:           8
        .value_kind:     global_buffer
      - .actual_access:  read_only
        .address_space:  global
        .offset:         16
        .size:           8
        .value_kind:     global_buffer
      - .actual_access:  read_only
        .address_space:  global
        .offset:         24
        .size:           8
        .value_kind:     global_buffer
      - .actual_access:  read_only
        .address_space:  global
        .offset:         32
        .size:           8
        .value_kind:     global_buffer
      - .actual_access:  read_only
        .address_space:  global
        .offset:         40
        .size:           8
        .value_kind:     global_buffer
      - .actual_access:  read_only
        .address_space:  global
        .offset:         48
        .size:           8
        .value_kind:     global_buffer
      - .actual_access:  write_only
        .address_space:  global
        .offset:         56
        .size:           8
        .value_kind:     global_buffer
    .group_segment_fixed_size: 145952
    .kernarg_segment_align: 8
    .kernarg_segment_size: 64
    .language:       OpenCL C
    .language_version:
      - 2
      - 0
    .max_flat_workgroup_size: 512
    .name:           _Z7k_finalPK15HIP_vector_typeIfLj4EES2_PKiS4_PKfS6_PKDF16_Pf
    .private_segment_fixed_size: 0
    .sgpr_count:     34
    .sgpr_spill_count: 0
    .symbol:         _Z7k_finalPK15HIP_vector_typeIfLj4EES2_PKiS4_PKfS6_PKDF16_Pf.kd
    .uniform_work_group_size: 1
    .uses_dynamic_stack: false
    .vgpr_count:     177
    .vgpr_spill_count: 0
    .wavefront_size: 64
  - .agpr_count:     0
    .args:
      - .actual_access:  read_only
        .address_space:  global
        .offset:         0
        .size:           8
        .value_kind:     global_buffer
      - .actual_access:  read_only
        .address_space:  global
        .offset:         8
        .size:           8
        .value_kind:     global_buffer
      - .actual_access:  read_only
        .address_space:  global
        .offset:         16
        .size:           8
        .value_kind:     global_buffer
      - .actual_access:  read_only
        .address_space:  global
        .offset:         24
        .size:           8
        .value_kind:     global_buffer
      - .actual_access:  read_only
        .address_space:  global
        .offset:         32
        .size:           8
        .value_kind:     global_buffer
      - .actual_access:  read_only
        .address_space:  global
        .offset:         40
        .size:           8
        .value_kind:     global_buffer
      - .actual_access:  read_only
        .address_space:  global
        .offset:         48
        .size:           8
        .value_kind:     global_buffer
      - .actual_access:  read_only
        .address_space:  global
        .offset:         56
        .size:           8
        .value_kind:     global_buffer
      - .actual_access:  read_only
        .address_space:  global
        .offset:         64
        .size:           8
        .value_kind:     global_buffer
      - .address_space:  global
        .offset:         72
        .size:           8
        .value_kind:     global_buffer
      - .actual_access:  read_only
        .address_space:  global
        .offset:         80
        .size:           8
        .value_kind:     global_buffer
      - .actual_access:  read_only
        .address_space:  global
        .offset:         88
        .size:           8
        .value_kind:     global_buffer
      - .actual_access:  read_only
        .address_space:  global
        .offset:         96
        .size:           8
        .value_kind:     global_buffer
      - .actual_access:  write_only
        .address_space:  global
        .offset:         104
        .size:           8
        .value_kind:     global_buffer
      - .address_space:  global
        .offset:         112
        .size:           8
        .value_kind:     global_buffer
      - .actual_access:  write_only
        .address_space:  global
        .offset:         120
        .size:           8
        .value_kind:     global_buffer
      - .actual_access:  write_only
        .address_space:  global
        .offset:         128
        .size:           8
        .value_kind:     global_buffer
      - .actual_access:  write_only
        .address_space:  global
        .offset:         136
        .size:           8
        .value_kind:     global_buffer
      - .actual_access:  write_only
        .address_space:  global
        .offset:         144
        .size:           8
        .value_kind:     global_buffer
    .group_segment_fixed_size: 30384
    .kernarg_segment_align: 8
    .kernarg_segment_size: 152
    .language:       OpenCL C
    .language_version:
      - 2
      - 0
    .max_flat_workgroup_size: 512
    .name:           _Z6k_iterILb1ELb0EEvPKfS1_PKiPK15HIP_vector_typeIfLj4EES7_S1_S1_S3_S1_PfS8_S1_S3_PDF16_PS5_SA_PiSA_SB_
    .private_segment_fixed_size: 0
    .sgpr_count:     108
    .sgpr_spill_count: 0
    .symbol:         _Z6k_iterILb1ELb0EEvPKfS1_PKiPK15HIP_vector_typeIfLj4EES7_S1_S1_S3_S1_PfS8_S1_S3_PDF16_PS5_SA_PiSA_SB_.kd
    .uniform_work_group_size: 1
    .uses_dynamic_stack: false
    .vgpr_count:     256
    .vgpr_spill_count: 0
    .wavefront_size: 64
  - .agpr_count:     0
    .args:
      - .actual_access:  read_only
        .address_space:  global
        .offset:         0
        .size:           8
        .value_kind:     global_buffer
      - .actual_access:  read_only
        .address_space:  global
        .offset:         8
        .size:           8
        .value_kind:     global_buffer
      - .actual_access:  read_only
        .address_space:  global
        .offset:         16
        .size:           8
        .value_kind:     global_buffer
      - .actual_access:  read_only
        .address_space:  global
        .offset:         24
        .size:           8
        .value_kind:     global_buffer
      - .actual_access:  read_only
        .address_space:  global
        .offset:         32
        .size:           8
        .value_kind:     global_buffer
      - .actual_access:  read_only
        .address_space:  global
        .offset:         40
        .size:           8
        .value_kind:     global_buffer
      - .actual_access:  read_only
        .address_space:  global
        .offset:         48
        .size:           8
        .value_kind:     global_buffer
      - .actual_access:  read_only
        .address_space:  global
        .offset:         56
        .size:           8
        .value_kind:     global_buffer
      - .actual_access:  read_only
        .address_space:  global
        .offset:         64
        .size:           8
        .value_kind:     global_buffer
      - .address_space:  global
        .offset:         72
        .size:           8
        .value_kind:     global_buffer
      - .actual_access:  read_only
        .address_space:  global
        .offset:         80
        .size:           8
        .value_kind:     global_buffer
      - .actual_access:  read_only
        .address_space:  global
        .offset:         88
        .size:           8
        .value_kind:     global_buffer
      - .actual_access:  read_only
        .address_space:  global
        .offset:         96
        .size:           8
        .value_kind:     global_buffer
      - .actual_access:  read_only
        .address_space:  global
        .offset:         104
        .size:           8
        .value_kind:     global_buffer
      - .actual_access:  read_only
        .address_space:  global
        .offset:         112
        .size:           8
        .value_kind:     global_buffer
      - .actual_access:  read_only
        .address_space:  global
        .offset:         120
        .size:           8
        .value_kind:     global_buffer
      - .actual_access:  read_only
        .address_space:  global
        .offset:         128
        .size:           8
        .value_kind:     global_buffer
      - .actual_access:  read_only
        .address_space:  global
        .offset:         136
        .size:           8
        .value_kind:     global_buffer
      - .actual_access:  read_only
        .address_space:  global
        .offset:         144
        .size:           8
        .value_kind:     global_buffer
    .group_segment_fixed_size: 5808
    .kernarg_segment_align: 8
    .kernarg_segment_size: 152
    .language:       OpenCL C
    .language_version:
      - 2
      - 0
    .max_flat_workgroup_size: 512
    .name:           _Z6k_iterILb0ELb0EEvPKfS1_PKiPK15HIP_vector_typeIfLj4EES7_S1_S1_S3_S1_PfS8_S1_S3_PDF16_PS5_SA_PiSA_SB_
    .private_segment_fixed_size: 0
    .sgpr_count:     46
    .sgpr_spill_count: 0
    .symbol:         _Z6k_iterILb0ELb0EEvPKfS1_PKiPK15HIP_vector_typeIfLj4EES7_S1_S1_S3_S1_PfS8_S1_S3_PDF16_PS5_SA_PiSA_SB_.kd
    .uniform_work_group_size: 1
    .uses_dynamic_stack: false
    .vgpr_count:     184
    .vgpr_spill_count: 0
    .wavefront_size: 64
  - .agpr_count:     0
    .args:
      - .actual_access:  read_only
        .address_space:  global
        .offset:         0
        .size:           8
        .value_kind:     global_buffer
      - .actual_access:  read_only
        .address_space:  global
        .offset:         8
        .size:           8
        .value_kind:     global_buffer
      - .actual_access:  read_only
        .address_space:  global
        .offset:         16
        .size:           8
        .value_kind:     global_buffer
      - .actual_access:  read_only
        .address_space:  global
        .offset:         24
        .size:           8
        .value_kind:     global_buffer
      - .actual_access:  read_only
        .address_space:  global
        .offset:         32
        .size:           8
        .value_kind:     global_buffer
      - .actual_access:  read_only
        .address_space:  global
        .offset:         40
        .size:           8
        .value_kind:     global_buffer
      - .actual_access:  read_only
        .address_space:  global
        .offset:         48
        .size:           8
        .value_kind:     global_buffer
      - .actual_access:  read_only
        .address_space:  global
        .offset:         56
        .size:           8
        .value_kind:     global_buffer
      - .actual_access:  read_only
        .address_space:  global
        .offset:         64
        .size:           8
        .value_kind:     global_buffer
      - .address_space:  global
        .offset:         72
        .size:           8
        .value_kind:     global_buffer
      - .actual_access:  write_only
        .address_space:  global
        .offset:         80
        .size:           8
        .value_kind:     global_buffer
      - .actual_access:  read_only
        .address_space:  global
        .offset:         88
        .size:           8
        .value_kind:     global_buffer
      - .actual_access:  read_only
        .address_space:  global
        .offset:         96
        .size:           8
        .value_kind:     global_buffer
      - .actual_access:  read_only
        .address_space:  global
        .offset:         104
        .size:           8
        .value_kind:     global_buffer
      - .actual_access:  read_only
        .address_space:  global
        .offset:         112
        .size:           8
        .value_kind:     global_buffer
      - .actual_access:  read_only
        .address_space:  global
        .offset:         120
        .size:           8
        .value_kind:     global_buffer
      - .actual_access:  read_only
        .address_space:  global
        .offset:         128
        .size:           8
        .value_kind:     global_buffer
      - .actual_access:  read_only
        .address_space:  global
        .offset:         136
        .size:           8
        .value_kind:     global_buffer
      - .actual_access:  read_only
        .address_space:  global
        .offset:         144
        .size:           8
        .value_kind:     global_buffer
    .group_segment_fixed_size: 5808
    .kernarg_segment_align: 8
    .kernarg_segment_size: 152
    .language:       OpenCL C
    .language_version:
      - 2
      - 0
    .max_flat_workgroup_size: 512
    .name:           _Z6k_iterILb0ELb1EEvPKfS1_PKiPK15HIP_vector_typeIfLj4EES7_S1_S1_S3_S1_PfS8_S1_S3_PDF16_PS5_SA_PiSA_SB_
    .private_segment_fixed_size: 0
    .sgpr_count:     54
    .sgpr_spill_count: 0
    .symbol:         _Z6k_iterILb0ELb1EEvPKfS1_PKiPK15HIP_vector_typeIfLj4EES7_S1_S1_S3_S1_PfS8_S1_S3_PDF16_PS5_SA_PiSA_SB_.kd
    .uniform_work_group_size: 1
    .uses_dynamic_stack: false
    .vgpr_count:     184
    .vgpr_spill_count: 0
    .wavefront_size: 64
